# attention: K stream issued by waves 0-3 and V stream by waves 4-7, the four LDS-DMA pieces of each active wave spread into MFMA gaps of the QK phase instead of back-to-back after the barrier (VMEM iss
# baseline (speedup 1.0000x reference)
.LBB0_1088:
	v_lshlrev_b32_e32 v13, 3, v146
	v_and_b32_e32 v12, 0xc0, v12
	v_lshlrev_b32_e32 v14, 1, v146
	s_xor_b64 s[34:35], s[4:5], -1
	v_and_or_b32 v12, v13, 24, v12
	v_and_b32_e32 v14, 32, v14
	v_and_b32_e32 v13, 0x100, v13
	s_add_i32 s44, s44, s8
	v_or3_b32 v12, v12, v14, v13
	v_or_b32_e32 v13, s44, v145
	s_cmp_lg_u32 0, -1
	s_cselect_b32 s4, 0, 0
	s_lshr_b32 s46, s7, 6
	v_add_u32_e32 v163, 0xffffff91, v13
	v_lshlrev_b32_e32 v164, 4, v4
	v_lshlrev_b32_e32 v13, 4, v145
	s_add_i32 s38, 0, 0x10800
	s_add_i32 s47, s46, -2
	s_or_b32 s64, s44, 31
	v_and_b32_e32 v13, 0x70, v13
	v_add_u32_e32 v14, 32, v164
	v_lshl_add_u32 v171, v146, 2, s38
	s_lshl_b32 s38, s46, 8
	v_xad_u32 v168, v14, v13, 0
	v_add_u32_e32 v14, 64, v164
	s_add_u32 s38, s89, s38
	v_xad_u32 v169, v14, v13, 0
	v_add_u32_e32 v14, 0x60, v164
	s_addc_u32 s39, s88, 0
	s_and_b32 s7, s7, 0x1fc0
	s_add_i32 s6, s60, s6
	v_lshlrev_b32_e32 v144, 2, v4
	v_xad_u32 v166, v13, v164, 0
	v_xad_u32 v170, v14, v13, 0
	s_sub_i32 s65, s7, 64
	v_add_u32_e32 v13, s6, v145
	s_lshl_b32 s6, s46, 18
	v_ashrrev_i32_e32 v147, 31, v146
	v_sub_u32_e32 v13, v13, v144
	s_add_u32 s6, s90, s6
	v_lshl_add_u64 v[148:149], v[146:147], 2, s[38:39]
	v_subrev_u32_e32 v147, s7, v13
	s_addc_u32 s7, s91, 0
	v_add_u32_e32 v0, v0, v10
	v_lshl_add_u64 v[150:151], s[6:7], 0, v[0:1]
	v_add3_u32 v0, s61, v6, v11
	v_lshl_add_u64 v[152:153], s[6:7], 0, v[0:1]
	v_add_u32_e32 v0, v7, v5
	v_add3_u32 v0, v0, v8, v2
	v_lshl_or_b32 v0, v0, 12, v9
	v_add_u32_e32 v0, v0, v3
	v_lshl_add_u64 v[154:155], s[6:7], 0, v[0:1]
	v_add_u32_e32 v0, s62, v4
	v_lshlrev_b32_e32 v4, 1, v0
	s_mov_b32 s38, 0xffff0
	v_and_or_b32 v4, v4, s38, v5
	v_and_b32_e32 v0, 4, v0
	v_add_u32_e32 v162, s4, v12
	v_lshrrev_b32_e32 v12, 5, v146
	v_add_u32_e32 v0, v4, v0
	v_add_lshl_u32 v0, v0, v2, 12
	v_add_u16_e32 v2, 2, v12
	v_and_b32_e32 v2, 3, v2
	v_lshlrev_b32_e32 v2, 6, v2
	s_waitcnt vmcnt(0)
	v_or3_b32 v0, v0, v2, v3
	v_mov_b32_e32 v14, v1
	v_mov_b32_e32 v15, v1
	v_lshl_add_u64 v[156:157], s[6:7], 0, v[0:1]
	v_mov_b32_e32 v0, v1
	v_mov_b32_e32 v2, v1
	v_mov_b32_e32 v3, v1
	v_mov_b32_e32 v4, v1
	v_mov_b32_e32 v5, v1
	v_mov_b32_e32 v6, v1
	v_mov_b32_e32 v7, v1
	v_mov_b32_e32 v8, v1
	v_mov_b32_e32 v9, v1
	v_mov_b32_e32 v10, v1
	v_mov_b32_e32 v11, v1
	v_mov_b32_e32 v12, v1
	v_mov_b32_e32 v13, v1
	s_waitcnt lgkmcnt(0)
	v_mov_b64_e32 v[30:31], v[14:15]
	v_mov_b64_e32 v[46:47], v[14:15]
	v_mov_b64_e32 v[62:63], v[14:15]
	v_mov_b64_e32 v[78:79], v[14:15]
	s_mov_b32 s45, 0
	v_lshlrev_b32_e32 v165, 8, v145
	v_cmp_gt_u32_e64 s[4:5], 32, v146
	v_lshl_add_u32 v167, v145, 2, s54
	v_add_u32_e32 v161, s54, v164
	v_mov_b32_e32 v174, 0
	v_mov_b32_e32 v173, 0xf149f2ca
	s_mov_b32 s66, s46
	v_mov_b64_e32 v[28:29], v[12:13]
	v_mov_b64_e32 v[26:27], v[10:11]
	v_mov_b64_e32 v[24:25], v[8:9]
	v_mov_b64_e32 v[22:23], v[6:7]
	v_mov_b64_e32 v[20:21], v[4:5]
	v_mov_b64_e32 v[18:19], v[2:3]
	v_mov_b64_e32 v[16:17], v[0:1]
	v_mov_b64_e32 v[44:45], v[12:13]
	v_mov_b64_e32 v[42:43], v[10:11]
	v_mov_b64_e32 v[40:41], v[8:9]
	v_mov_b64_e32 v[38:39], v[6:7]
	v_mov_b64_e32 v[36:37], v[4:5]
	v_mov_b64_e32 v[34:35], v[2:3]
	v_mov_b64_e32 v[32:33], v[0:1]
	v_mov_b64_e32 v[60:61], v[12:13]
	v_mov_b64_e32 v[58:59], v[10:11]
	v_mov_b64_e32 v[56:57], v[8:9]
	v_mov_b64_e32 v[54:55], v[6:7]
	v_mov_b64_e32 v[52:53], v[4:5]
	v_mov_b64_e32 v[50:51], v[2:3]
	v_mov_b64_e32 v[48:49], v[0:1]
	v_mov_b64_e32 v[76:77], v[12:13]
	v_mov_b64_e32 v[74:75], v[10:11]
	v_mov_b64_e32 v[72:73], v[8:9]
	v_mov_b64_e32 v[70:71], v[6:7]
	v_mov_b64_e32 v[68:69], v[4:5]
	v_mov_b64_e32 v[66:67], v[2:3]
	v_mov_b64_e32 v[64:65], v[0:1]
	s_waitcnt vmcnt(0)
	s_barrier
	s_mov_b32 s45, 0
	s_lshl_b32 s65, s46, 6
	s_mov_b32 s66, 0
	s_mov_b32 s33, 0x8000
	s_mov_b32 s42, 0x11000
	s_mov_b32 s43, 0x15000
	s_mov_b32 s47, 0x19000
	s_mov_b32 s99, 0
	v_subrev_u32_e32 v147, 64, v147
	v_lshlrev_b32_e32 v232, 2, v146
	s_lshr_b32 s6, s68, 11
	s_and_b32 s7, s6, 3
	s_lshl_b32 s98, s7, 12
	s_lshl_b32 s7, s7, 16
	s_add_i32 s40, s46, -1
	s_lshl_b32 s41, s40, 8
	s_lshl_b32 s39, s40, 18
	s_add_u32 s40, s30, s41
	s_addc_u32 s41, s31, 0
	s_add_u32 s39, s39, s7
	v_and_b32_e32 v0, 15, v145
	v_lshlrev_b32_e32 v0, 4, v0
	v_xor_b32_e32 v0, v0, v164
	v_xad_u32 v166, v0, 0, v165
	v_xad_u32 v168, v0, 32, v165
	v_xad_u32 v169, v0, 64, v165
	s_movk_i32 s7, 0x60
	v_xad_u32 v170, v0, s7, v165
	s_movk_i32 s7, 0x80
	v_xad_u32 v251, v0, s7, v165
	s_movk_i32 s7, 0xa0
	v_xad_u32 v252, v0, s7, v165
	s_movk_i32 s7, 0xc0
	v_xad_u32 v253, v0, s7, v165
	s_movk_i32 s7, 0xe0
	v_xad_u32 v254, v0, s7, v165
	s_cmp_ge_u32 s6, 4
	s_cbranch_scc1 .Lat_setup_b
	s_add_u32 s38, s82, s39
	s_addc_u32 s39, s83, 0
	v_lshrrev_b32_e32 v0, 4, v146
	v_and_b32_e32 v2, 15, v146
	v_xor_b32_e32 v2, v2, v0
	v_lshlrev_b32_e32 v2, 4, v2
	v_lshl_add_u32 v228, v0, 12, v2
	v_xor_b32_e32 v229, 0x40, v228
	v_add_u32_e32 v229, 0x4000, v229
	v_xor_b32_e32 v230, 0x80, v228
	v_add_u32_e32 v230, 0x8000, v230
	v_xor_b32_e32 v231, 0xc0, v228
	v_add_u32_e32 v231, 0xc000, v231
	s_add_i32 s6, s42, s98
	s_mov_b32 s7, s6
	s_mov_b32 m0, s7
	s_add_i32 s7, s7, 0x400
	global_load_lds_dwordx4 v228, s[38:39]
	s_mov_b32 m0, s7
	s_add_i32 s7, s7, 0x400
	global_load_lds_dwordx4 v229, s[38:39]
	s_mov_b32 m0, s7
	s_add_i32 s7, s7, 0x400
	global_load_lds_dwordx4 v230, s[38:39]
	s_mov_b32 m0, s7
	s_nop 0
	global_load_lds_dwordx4 v231, s[38:39]
	global_load_dword v154, v232, s[40:41]
	s_sub_u32 s38, s38, 0x40000
	s_subb_u32 s39, s39, 0
	s_sub_u32 s40, s40, 0x100
	s_subb_u32 s41, s41, 0
	s_add_i32 s6, s43, s98
	s_mov_b32 s7, s6
	s_mov_b32 m0, s7
	s_add_i32 s7, s7, 0x400
	global_load_lds_dwordx4 v228, s[38:39]
	s_mov_b32 m0, s7
	s_add_i32 s7, s7, 0x400
	global_load_lds_dwordx4 v229, s[38:39]
	s_mov_b32 m0, s7
	s_add_i32 s7, s7, 0x400
	global_load_lds_dwordx4 v230, s[38:39]
	s_mov_b32 m0, s7
	s_nop 0
	global_load_lds_dwordx4 v231, s[38:39]
	global_load_dword v172, v232, s[40:41]
	s_sub_u32 s38, s38, 0x40000
	s_subb_u32 s39, s39, 0
	s_sub_u32 s40, s40, 0x100
	s_subb_u32 s41, s41, 0
	s_add_i32 s6, s47, s98
	s_mov_b32 s7, s6
	s_mov_b32 m0, s7
	s_add_i32 s7, s7, 0x400
	global_load_lds_dwordx4 v228, s[38:39]
	s_mov_b32 m0, s7
	s_add_i32 s7, s7, 0x400
	global_load_lds_dwordx4 v229, s[38:39]
	s_mov_b32 m0, s7
	s_add_i32 s7, s7, 0x400
	global_load_lds_dwordx4 v230, s[38:39]
	s_mov_b32 m0, s7
	s_nop 0
	global_load_lds_dwordx4 v231, s[38:39]
	global_load_dword v156, v232, s[40:41]
	s_sub_u32 s38, s38, 0x40000
	s_subb_u32 s39, s39, 0
	s_sub_u32 s40, s40, 0x100
	s_subb_u32 s41, s41, 0
	s_waitcnt vmcnt(0)
	s_and_b64 vcc, exec, s[2:3]
	s_cbranch_vccnz .Lat_setup_done
	v_add_u32_e32 v0, 256, v171
	ds_write_b32 v0, v154
	v_add_u32_e32 v0, 512, v171
	ds_write_b32 v0, v172
	v_add_u32_e32 v0, 768, v171
	ds_write_b32 v0, v156
	s_waitcnt lgkmcnt(0)
	s_branch .Lat_setup_done
.Lat_setup_b:
	s_add_u32 s38, s84, s39
	s_addc_u32 s39, s85, 0
	v_bfe_u32 v0, v146, 4, 1
	v_bfe_u32 v2, v146, 2, 2
	v_lshl_add_u32 v0, v0, 3, v2
	v_lshlrev_b32_e32 v0, 12, v0
	v_lshrrev_b32_e32 v2, 5, v146
	v_lshl_add_u32 v0, v2, 6, v0
	v_and_b32_e32 v2, 3, v146
	v_lshl_add_u32 v228, v2, 4, v0
	v_add_u32_e32 v229, 0x80, v228
	v_add_u32_e32 v230, 0x4000, v228
	v_add_u32_e32 v231, 0x4080, v228
	s_add_i32 s6, s98, 0x4000
	s_mov_b32 s7, s6
	s_mov_b32 m0, s7
	s_add_i32 s7, s7, 0x400
	global_load_lds_dwordx4 v228, s[38:39]
	s_mov_b32 m0, s7
	s_add_i32 s7, s7, 0x400
	global_load_lds_dwordx4 v229, s[38:39]
	s_mov_b32 m0, s7
	s_add_i32 s7, s7, 0x400
	global_load_lds_dwordx4 v230, s[38:39]
	s_mov_b32 m0, s7
	s_nop 0
	global_load_lds_dwordx4 v231, s[38:39]
	s_sub_u32 s38, s38, 0x40000
	s_subb_u32 s39, s39, 0

.Lat_tile0:
	s_waitcnt lgkmcnt(0)
	s_barrier
	s_cmp_ge_u32 s68, 0x2000
	s_cbranch_scc0 .Lat_adma0
	s_add_i32 s6, s45, 2
	s_cmp_ge_u32 s6, s46
	s_cbranch_scc1 .Lat_go0
	s_cmp_eq_u32 s66, 0
	s_cselect_b32 s6, 0xc000, 0
	s_cmp_eq_u32 s66, 0xc000
	s_cselect_b32 s6, 0x4000, s6
	s_add_i32 s6, s6, s98
	s_branch .Lat_dsel0
.Lat_adma0:
	s_add_i32 s6, s45, 4
	s_cmp_ge_u32 s6, s46
	s_cbranch_scc1 .Lat_go0
	global_load_dword v172, v232, s[40:41]
	s_add_i32 s6, s33, s98
.Lat_dsel0:
	s_cmp_gt_i32 s65, s64
	s_cbranch_scc0 .Lat_steady0s
	s_mov_b32 s7, s6
	s_mov_b32 m0, s7
	s_add_i32 s7, s7, 0x400
	global_load_lds_dwordx4 v228, s[38:39]
	s_mov_b32 m0, s7
	s_add_i32 s7, s7, 0x400
	global_load_lds_dwordx4 v229, s[38:39]
	s_mov_b32 m0, s7
	s_add_i32 s7, s7, 0x400
	global_load_lds_dwordx4 v230, s[38:39]
	s_mov_b32 m0, s7
	s_nop 0
	global_load_lds_dwordx4 v231, s[38:39]
	s_branch .Lat_go0
.Lat_steady0s:
	s_waitcnt lgkmcnt(0)
	v_add_u32_e32 v246, s42, v251
	v_add_u32_e32 v247, s42, v252
	v_add_u32_e32 v248, s42, v253
	v_add_u32_e32 v249, s42, v254
	v_add_u32_e32 v153, s66, v162
	v_mfma_f32_32x32x16_bf16 v[176:191], v[208:211], v[112:115], v[176:191]
	ds_read_b128 v[208:211], v246
	v_exp_f32_e32 v80, v80
	v_exp_f32_e32 v81, v81
	v_add_f32_e32 v148, v96, v100
	v_add_f32_e32 v149, v97, v101
	v_mfma_f32_32x32x16_bf16 v[192:207], v[212:215], v[112:115], v[192:207]
	ds_read_b128 v[212:215], v246 offset:8192
	s_mov_b32 m0, s6
	s_add_i32 s6, s6, 0x400
	global_load_lds_dwordx4 v228, s[38:39]
	v_exp_f32_e32 v82, v82
	v_exp_f32_e32 v83, v83
	v_add_f32_e32 v150, v98, v102
	v_add_f32_e32 v151, v99, v103
	v_mfma_f32_32x32x16_bf16 v[176:191], v[216:219], v[116:119], v[176:191]
	ds_read_b128 v[216:219], v247
	v_exp_f32_e32 v84, v84
	v_exp_f32_e32 v85, v85
	v_add_f32_e32 v148, v148, v104
	v_add_f32_e32 v149, v149, v105
	v_mfma_f32_32x32x16_bf16 v[192:207], v[220:223], v[116:119], v[192:207]
	ds_read_b128 v[220:223], v247 offset:8192
	v_exp_f32_e32 v86, v86
	v_exp_f32_e32 v87, v87
	v_add_f32_e32 v150, v150, v106
	v_add_f32_e32 v151, v151, v107
	v_mfma_f32_32x32x16_bf16 v[176:191], v[224:227], v[120:123], v[176:191]
	ds_read_b128 v[224:227], v248
	v_exp_f32_e32 v88, v88
	v_exp_f32_e32 v89, v89
	v_add_f32_e32 v148, v148, v108
	v_add_f32_e32 v149, v149, v109
	v_mfma_f32_32x32x16_bf16 v[192:207], v[234:237], v[120:123], v[192:207]
	ds_read_b128 v[234:237], v248 offset:8192
	s_mov_b32 m0, s6
	s_add_i32 s6, s6, 0x400
	global_load_lds_dwordx4 v229, s[38:39]
	v_exp_f32_e32 v90, v90
	v_exp_f32_e32 v91, v91
	v_add_f32_e32 v150, v150, v110
	v_add_f32_e32 v151, v151, v111
	v_mfma_f32_32x32x16_bf16 v[176:191], v[238:241], v[124:127], v[176:191]
	ds_read_b128 v[238:241], v249
	v_exp_f32_e32 v92, v92
	v_exp_f32_e32 v93, v93
	v_add_f32_e32 v148, v148, v80
	v_add_f32_e32 v149, v149, v81
	v_mfma_f32_32x32x16_bf16 v[192:207], v[242:245], v[124:127], v[192:207]
	ds_read_b128 v[242:245], v249 offset:8192
	v_exp_f32_e32 v94, v94
	v_exp_f32_e32 v95, v95
	v_add_f32_e32 v150, v150, v82
	v_add_f32_e32 v151, v151, v83
	s_waitcnt lgkmcnt(7)
	v_mfma_f32_32x32x16_bf16 v[176:191], v[208:211], v[128:131], v[176:191]
	ds_read_b64_tr_b16 v[208:209], v153 offset:0
	ds_read_b64_tr_b16 v[210:211], v153 offset:2048
	v_add_f32_e32 v148, v148, v84
	v_add_f32_e32 v149, v149, v85
	v_add_f32_e32 v150, v150, v86
	v_add_f32_e32 v151, v151, v87
	v_add_f32_e32 v148, v148, v88
	v_add_f32_e32 v149, v149, v89
	s_waitcnt lgkmcnt(8)
	v_mfma_f32_32x32x16_bf16 v[192:207], v[212:215], v[128:131], v[192:207]
	ds_read_b64_tr_b16 v[212:213], v153 offset:512
	ds_read_b64_tr_b16 v[214:215], v153 offset:2560
	s_mov_b32 m0, s6
	s_add_i32 s6, s6, 0x400
	global_load_lds_dwordx4 v230, s[38:39]
	v_add_f32_e32 v150, v150, v90
	v_add_f32_e32 v151, v151, v91
	v_add_f32_e32 v148, v148, v92
	v_add_f32_e32 v149, v149, v93
	v_add_f32_e32 v150, v150, v94
	v_add_f32_e32 v151, v151, v95
	s_waitcnt lgkmcnt(9)
	v_mfma_f32_32x32x16_bf16 v[176:191], v[216:219], v[132:135], v[176:191]
	ds_read_b64_tr_b16 v[216:217], v153 offset:1024
	ds_read_b64_tr_b16 v[218:219], v153 offset:3072
	v_add_f32_e32 v148, v148, v149
	v_add_f32_e32 v150, v150, v151
	v_add_f32_e32 v148, v148, v150
	v_mov_b32_e32 v152, v148
	v_cvt_pk_bf16_f32 v96, v96, v97
	v_cvt_pk_bf16_f32 v97, v98, v99
	s_waitcnt lgkmcnt(10)
	v_mfma_f32_32x32x16_bf16 v[192:207], v[220:223], v[132:135], v[192:207]
	ds_read_b64_tr_b16 v[220:221], v153 offset:1536
	ds_read_b64_tr_b16 v[222:223], v153 offset:3584
	v_permlane32_swap_b32_e32 v148, v152
	v_cvt_pk_bf16_f32 v98, v100, v101
	v_cvt_pk_bf16_f32 v99, v102, v103
	v_add_f32_e32 v148, v148, v152
	v_cvt_pk_bf16_f32 v100, v104, v105
	v_cvt_pk_bf16_f32 v101, v106, v107
	s_waitcnt lgkmcnt(11)
	v_mfma_f32_32x32x16_bf16 v[176:191], v[224:227], v[136:139], v[176:191]
	ds_read_b64_tr_b16 v[224:225], v153 offset:4096
	ds_read_b64_tr_b16 v[226:227], v153 offset:6144
	v_cvt_pk_bf16_f32 v102, v108, v109
	v_cvt_pk_bf16_f32 v103, v110, v111
	v_cvt_pk_bf16_f32 v104, v80, v81
	v_cvt_pk_bf16_f32 v105, v82, v83
	v_cvt_pk_bf16_f32 v106, v84, v85
	v_cvt_pk_bf16_f32 v107, v86, v87
	s_waitcnt lgkmcnt(12)
	v_mfma_f32_32x32x16_bf16 v[192:207], v[234:237], v[136:139], v[192:207]
	ds_read_b64_tr_b16 v[234:235], v153 offset:4608
	ds_read_b64_tr_b16 v[236:237], v153 offset:6656
	s_mov_b32 m0, s6
	s_add_i32 s6, s6, 0x400
	global_load_lds_dwordx4 v231, s[38:39]
	v_cvt_pk_bf16_f32 v108, v88, v89
	v_cvt_pk_bf16_f32 v109, v90, v91
	v_cvt_pk_bf16_f32 v110, v92, v93
	v_cvt_pk_bf16_f32 v111, v94, v95
	v_fma_f32 v174, v174, v233, v148
	s_nop 0
	s_waitcnt lgkmcnt(13)
	v_mfma_f32_32x32x16_bf16 v[176:191], v[238:241], v[140:143], v[176:191]
	ds_read_b64_tr_b16 v[238:239], v153 offset:5120
	ds_read_b64_tr_b16 v[240:241], v153 offset:7168
	v_permlane32_swap_b32_e32 v96, v98
	v_permlane32_swap_b32_e32 v97, v99
	v_permlane32_swap_b32_e32 v100, v102
	v_permlane32_swap_b32_e32 v101, v103
	v_permlane32_swap_b32_e32 v104, v106
	v_permlane32_swap_b32_e32 v105, v107
	s_waitcnt lgkmcnt(14)
	v_mfma_f32_32x32x16_bf16 v[192:207], v[242:245], v[140:143], v[192:207]
	ds_read_b64_tr_b16 v[242:243], v153 offset:5632
	ds_read_b64_tr_b16 v[244:245], v153 offset:7680
	v_permlane32_swap_b32_e32 v108, v110
	v_permlane32_swap_b32_e32 v109, v111
	s_add_i32 s6, s65, -1
	s_cmp_gt_i32 s6, s44
	s_cbranch_scc1 .Lat_mask0s
	s_cmp_lt_i32 s65, 0xb0
	s_cbranch_scc0 .Lat_nomask0s

.Lat_p2last0s:
	s_waitcnt lgkmcnt(14)
	v_mfma_f32_32x32x16_bf16 v[64:79], v[96:99], v[208:211], v[64:79]
	ds_read_b64_tr_b16 v[208:209], v153 offset:8192
	ds_read_b64_tr_b16 v[210:211], v153 offset:10240
	ds_read_b128 v[80:83], v152 offset:128
	s_waitcnt lgkmcnt(15)
	v_mfma_f32_32x32x16_bf16 v[48:63], v[96:99], v[212:215], v[48:63]
	ds_read_b64_tr_b16 v[212:213], v153 offset:8704
	ds_read_b64_tr_b16 v[214:215], v153 offset:10752
	ds_read_b128 v[84:87], v152 offset:160
	s_waitcnt lgkmcnt(15)
	v_mfma_f32_32x32x16_bf16 v[32:47], v[96:99], v[216:219], v[32:47]
	ds_read_b64_tr_b16 v[216:217], v153 offset:9216
	ds_read_b64_tr_b16 v[218:219], v153 offset:11264
	ds_read_b128 v[88:91], v152 offset:192
	s_waitcnt lgkmcnt(15)
	v_mfma_f32_32x32x16_bf16 v[16:31], v[96:99], v[220:223], v[16:31]
	ds_read_b64_tr_b16 v[220:221], v153 offset:9728
	ds_read_b64_tr_b16 v[222:223], v153 offset:11776
	ds_read_b128 v[92:95], v152 offset:224
	ds_read_b128 v[96:99], v152
	s_waitcnt lgkmcnt(15)
	v_mfma_f32_32x32x16_bf16 v[64:79], v[100:103], v[224:227], v[64:79]
	ds_read_b64_tr_b16 v[224:225], v153 offset:12288
	ds_read_b64_tr_b16 v[226:227], v153 offset:14336
	s_waitcnt lgkmcnt(15)
	v_mfma_f32_32x32x16_bf16 v[48:63], v[100:103], v[234:237], v[48:63]
	ds_read_b64_tr_b16 v[234:235], v153 offset:12800
	ds_read_b64_tr_b16 v[236:237], v153 offset:14848
	s_waitcnt lgkmcnt(15)
	v_mfma_f32_32x32x16_bf16 v[32:47], v[100:103], v[238:241], v[32:47]
	ds_read_b64_tr_b16 v[238:239], v153 offset:13312
	ds_read_b64_tr_b16 v[240:241], v153 offset:15360
	s_waitcnt lgkmcnt(15)
	v_mfma_f32_32x32x16_bf16 v[16:31], v[100:103], v[242:245], v[16:31]
	ds_read_b64_tr_b16 v[242:243], v153 offset:13824
	ds_read_b64_tr_b16 v[244:245], v153 offset:15872
	ds_read_b128 v[100:103], v152 offset:32
	s_waitcnt lgkmcnt(15)
	v_mfma_f32_32x32x16_bf16 v[64:79], v[104:107], v[208:211], v[64:79]
	ds_read_b128 v[208:211], v246
	s_waitcnt lgkmcnt(15)
	v_mfma_f32_32x32x16_bf16 v[48:63], v[104:107], v[212:215], v[48:63]
	ds_read_b128 v[212:215], v246 offset:8192
	s_waitcnt lgkmcnt(15)
	v_mfma_f32_32x32x16_bf16 v[32:47], v[104:107], v[216:219], v[32:47]
	ds_read_b128 v[216:219], v247
	s_waitcnt lgkmcnt(14)
	v_mfma_f32_32x32x16_bf16 v[16:31], v[104:107], v[220:223], v[16:31]
	ds_read_b128 v[220:223], v247 offset:8192
	ds_read_b128 v[104:107], v152 offset:64
	s_waitcnt lgkmcnt(12)
	v_mfma_f32_32x32x16_bf16 v[64:79], v[108:111], v[224:227], v[64:79]
	ds_read_b128 v[224:227], v248
	s_waitcnt lgkmcnt(11)
	v_mfma_f32_32x32x16_bf16 v[48:63], v[108:111], v[234:237], v[48:63]
	ds_read_b128 v[234:237], v248 offset:8192
	s_waitcnt lgkmcnt(10)
	v_mfma_f32_32x32x16_bf16 v[32:47], v[108:111], v[238:241], v[32:47]
	ds_read_b128 v[238:241], v249
	s_waitcnt lgkmcnt(9)
	v_mfma_f32_32x32x16_bf16 v[16:31], v[108:111], v[242:245], v[16:31]
	ds_read_b128 v[242:245], v249 offset:8192
	ds_read_b128 v[108:111], v152 offset:96
	s_branch .Lat_turn_end0

.Lat_turn_end0:
	s_add_i32 s45, s45, 1
	s_addk_i32 s65, 0xffc0
	s_cmp_eq_u32 s66, 0
	s_cselect_b32 s7, 0x4000, 0
	s_cmp_eq_u32 s66, 0x4000
	s_cselect_b32 s66, 0xc000, s7
	v_add_u32_e32 v147, 64, v147
	s_sub_u32 s38, s38, 0x40000
	s_subb_u32 s39, s39, 0
	s_sub_u32 s100, s100, 0x40000
	s_subb_u32 s101, s101, 0
	s_sub_u32 s40, s40, 0x100
	s_subb_u32 s41, s41, 0
	s_mov_b32 s7, s33
	s_mov_b32 s33, s42
	s_mov_b32 s42, s43
	s_mov_b32 s43, s47
	s_mov_b32 s47, s7
	s_cmp_ge_u32 s68, 0x2000
	s_cbranch_scc0 .Lat_apost0
	s_add_i32 s6, s45, 1
	s_cmp_lt_u32 s6, s46
	s_cbranch_scc1 .Lat_w40
	s_waitcnt vmcnt(0)
	s_branch .Lat_next0
.Lat_w40:
	s_waitcnt vmcnt(4)
	s_branch .Lat_next0
.Lat_apost0:
	s_add_i32 s6, s45, 3
	s_cmp_lt_u32 s6, s46
	s_cbranch_scc1 .Lat_w50
	s_waitcnt vmcnt(0)
	s_branch .Lat_wd0
.Lat_w50:
	s_waitcnt vmcnt(5)
.Lat_wd0:
	s_and_b64 vcc, exec, s[2:3]
	s_cbranch_vccnz .Lat_next0
	s_add_i32 s6, s45, 2
	s_cmp_ge_u32 s6, s46
	s_cbranch_scc1 .Lat_next0
	s_and_b32 s7, s6, 3
	s_lshl_b32 s7, s7, 8
	v_add_u32_e32 v0, s7, v171
	ds_write_b32 v0, v156

.Lat_adma1:
	s_add_i32 s6, s45, 4
	s_cmp_ge_u32 s6, s46
	s_cbranch_scc1 .Lat_go1
	global_load_dword v156, v232, s[40:41]
	s_add_i32 s6, s33, s98

.Lat_steady1s:
	s_waitcnt lgkmcnt(0)
	v_add_u32_e32 v246, s42, v251
	v_add_u32_e32 v247, s42, v252
	v_add_u32_e32 v248, s42, v253
	v_add_u32_e32 v249, s42, v254
	v_add_u32_e32 v153, s66, v162
	v_mfma_f32_32x32x16_bf16 v[96:111], v[208:211], v[112:115], v[96:111]
	ds_read_b128 v[208:211], v246
	v_exp_f32_e32 v192, v192
	v_exp_f32_e32 v193, v193
	v_add_f32_e32 v148, v176, v180
	v_add_f32_e32 v149, v177, v181
	v_mfma_f32_32x32x16_bf16 v[80:95], v[212:215], v[112:115], v[80:95]
	ds_read_b128 v[212:215], v246 offset:8192
	s_mov_b32 m0, s6
	s_add_i32 s6, s6, 0x400
	global_load_lds_dwordx4 v228, s[38:39]
	v_exp_f32_e32 v194, v194
	v_exp_f32_e32 v195, v195
	v_add_f32_e32 v150, v178, v182
	v_add_f32_e32 v151, v179, v183
	v_mfma_f32_32x32x16_bf16 v[96:111], v[216:219], v[116:119], v[96:111]
	ds_read_b128 v[216:219], v247
	v_exp_f32_e32 v196, v196
	v_exp_f32_e32 v197, v197
	v_add_f32_e32 v148, v148, v184
	v_add_f32_e32 v149, v149, v185
	v_mfma_f32_32x32x16_bf16 v[80:95], v[220:223], v[116:119], v[80:95]
	ds_read_b128 v[220:223], v247 offset:8192
	v_exp_f32_e32 v198, v198
	v_exp_f32_e32 v199, v199
	v_add_f32_e32 v150, v150, v186
	v_add_f32_e32 v151, v151, v187
	v_mfma_f32_32x32x16_bf16 v[96:111], v[224:227], v[120:123], v[96:111]
	ds_read_b128 v[224:227], v248
	v_exp_f32_e32 v200, v200
	v_exp_f32_e32 v201, v201
	v_add_f32_e32 v148, v148, v188
	v_add_f32_e32 v149, v149, v189
	v_mfma_f32_32x32x16_bf16 v[80:95], v[234:237], v[120:123], v[80:95]
	ds_read_b128 v[234:237], v248 offset:8192
	s_mov_b32 m0, s6
	s_add_i32 s6, s6, 0x400
	global_load_lds_dwordx4 v229, s[38:39]
	v_exp_f32_e32 v202, v202
	v_exp_f32_e32 v203, v203
	v_add_f32_e32 v150, v150, v190
	v_add_f32_e32 v151, v151, v191
	v_mfma_f32_32x32x16_bf16 v[96:111], v[238:241], v[124:127], v[96:111]
	ds_read_b128 v[238:241], v249
	v_exp_f32_e32 v204, v204
	v_exp_f32_e32 v205, v205
	v_add_f32_e32 v148, v148, v192
	v_add_f32_e32 v149, v149, v193
	v_mfma_f32_32x32x16_bf16 v[80:95], v[242:245], v[124:127], v[80:95]
	ds_read_b128 v[242:245], v249 offset:8192
	v_exp_f32_e32 v206, v206
	v_exp_f32_e32 v207, v207
	v_add_f32_e32 v150, v150, v194
	v_add_f32_e32 v151, v151, v195
	s_waitcnt lgkmcnt(7)
	v_mfma_f32_32x32x16_bf16 v[96:111], v[208:211], v[128:131], v[96:111]
	ds_read_b64_tr_b16 v[208:209], v153 offset:0
	ds_read_b64_tr_b16 v[210:211], v153 offset:2048
	v_add_f32_e32 v148, v148, v196
	v_add_f32_e32 v149, v149, v197
	v_add_f32_e32 v150, v150, v198
	v_add_f32_e32 v151, v151, v199
	v_add_f32_e32 v148, v148, v200
	v_add_f32_e32 v149, v149, v201
	s_waitcnt lgkmcnt(8)
	v_mfma_f32_32x32x16_bf16 v[80:95], v[212:215], v[128:131], v[80:95]
	ds_read_b64_tr_b16 v[212:213], v153 offset:512
	ds_read_b64_tr_b16 v[214:215], v153 offset:2560
	s_mov_b32 m0, s6
	s_add_i32 s6, s6, 0x400
	global_load_lds_dwordx4 v230, s[38:39]
	v_add_f32_e32 v150, v150, v202
	v_add_f32_e32 v151, v151, v203
	v_add_f32_e32 v148, v148, v204
	v_add_f32_e32 v149, v149, v205
	v_add_f32_e32 v150, v150, v206
	v_add_f32_e32 v151, v151, v207
	s_waitcnt lgkmcnt(9)
	v_mfma_f32_32x32x16_bf16 v[96:111], v[216:219], v[132:135], v[96:111]
	ds_read_b64_tr_b16 v[216:217], v153 offset:1024
	ds_read_b64_tr_b16 v[218:219], v153 offset:3072
	v_add_f32_e32 v148, v148, v149
	v_add_f32_e32 v150, v150, v151
	v_add_f32_e32 v148, v148, v150
	v_mov_b32_e32 v152, v148
	v_cvt_pk_bf16_f32 v176, v176, v177
	v_cvt_pk_bf16_f32 v177, v178, v179
	s_waitcnt lgkmcnt(10)
	v_mfma_f32_32x32x16_bf16 v[80:95], v[220:223], v[132:135], v[80:95]
	ds_read_b64_tr_b16 v[220:221], v153 offset:1536
	ds_read_b64_tr_b16 v[222:223], v153 offset:3584
	v_permlane32_swap_b32_e32 v148, v152
	v_cvt_pk_bf16_f32 v178, v180, v181
	v_cvt_pk_bf16_f32 v179, v182, v183
	v_add_f32_e32 v148, v148, v152
	v_cvt_pk_bf16_f32 v180, v184, v185
	v_cvt_pk_bf16_f32 v181, v186, v187
	s_waitcnt lgkmcnt(11)
	v_mfma_f32_32x32x16_bf16 v[96:111], v[224:227], v[136:139], v[96:111]
	ds_read_b64_tr_b16 v[224:225], v153 offset:4096
	ds_read_b64_tr_b16 v[226:227], v153 offset:6144
	v_cvt_pk_bf16_f32 v182, v188, v189
	v_cvt_pk_bf16_f32 v183, v190, v191
	v_cvt_pk_bf16_f32 v184, v192, v193
	v_cvt_pk_bf16_f32 v185, v194, v195
	v_cvt_pk_bf16_f32 v186, v196, v197
	v_cvt_pk_bf16_f32 v187, v198, v199
	s_waitcnt lgkmcnt(12)
	v_mfma_f32_32x32x16_bf16 v[80:95], v[234:237], v[136:139], v[80:95]
	ds_read_b64_tr_b16 v[234:235], v153 offset:4608
	ds_read_b64_tr_b16 v[236:237], v153 offset:6656
	s_mov_b32 m0, s6
	s_add_i32 s6, s6, 0x400
	global_load_lds_dwordx4 v231, s[38:39]
	v_cvt_pk_bf16_f32 v188, v200, v201
	v_cvt_pk_bf16_f32 v189, v202, v203
	v_cvt_pk_bf16_f32 v190, v204, v205
	v_cvt_pk_bf16_f32 v191, v206, v207
	v_fma_f32 v174, v174, v233, v148
	s_nop 0
	s_waitcnt lgkmcnt(13)
	v_mfma_f32_32x32x16_bf16 v[96:111], v[238:241], v[140:143], v[96:111]
	ds_read_b64_tr_b16 v[238:239], v153 offset:5120
	ds_read_b64_tr_b16 v[240:241], v153 offset:7168
	v_permlane32_swap_b32_e32 v176, v178
	v_permlane32_swap_b32_e32 v177, v179
	v_permlane32_swap_b32_e32 v180, v182
	v_permlane32_swap_b32_e32 v181, v183
	v_permlane32_swap_b32_e32 v184, v186
	v_permlane32_swap_b32_e32 v185, v187
	s_waitcnt lgkmcnt(14)
	v_mfma_f32_32x32x16_bf16 v[80:95], v[242:245], v[140:143], v[80:95]
	ds_read_b64_tr_b16 v[242:243], v153 offset:5632
	ds_read_b64_tr_b16 v[244:245], v153 offset:7680
	v_permlane32_swap_b32_e32 v188, v190
	v_permlane32_swap_b32_e32 v189, v191
	s_add_i32 s6, s65, -1
	s_cmp_gt_i32 s6, s44
	s_cbranch_scc1 .Lat_mask1s
	s_cmp_lt_i32 s65, 0xb0
	s_cbranch_scc0 .Lat_nomask1s

.Lat_p2last1s:
	s_waitcnt lgkmcnt(14)
	v_mfma_f32_32x32x16_bf16 v[64:79], v[176:179], v[208:211], v[64:79]
	ds_read_b64_tr_b16 v[208:209], v153 offset:8192
	ds_read_b64_tr_b16 v[210:211], v153 offset:10240
	ds_read_b128 v[192:195], v152 offset:128
	s_waitcnt lgkmcnt(15)
	v_mfma_f32_32x32x16_bf16 v[48:63], v[176:179], v[212:215], v[48:63]
	ds_read_b64_tr_b16 v[212:213], v153 offset:8704
	ds_read_b64_tr_b16 v[214:215], v153 offset:10752
	ds_read_b128 v[196:199], v152 offset:160
	s_waitcnt lgkmcnt(15)
	v_mfma_f32_32x32x16_bf16 v[32:47], v[176:179], v[216:219], v[32:47]
	ds_read_b64_tr_b16 v[216:217], v153 offset:9216
	ds_read_b64_tr_b16 v[218:219], v153 offset:11264
	ds_read_b128 v[200:203], v152 offset:192
	s_waitcnt lgkmcnt(15)
	v_mfma_f32_32x32x16_bf16 v[16:31], v[176:179], v[220:223], v[16:31]
	ds_read_b64_tr_b16 v[220:221], v153 offset:9728
	ds_read_b64_tr_b16 v[222:223], v153 offset:11776
	ds_read_b128 v[204:207], v152 offset:224
	ds_read_b128 v[176:179], v152
	s_waitcnt lgkmcnt(15)
	v_mfma_f32_32x32x16_bf16 v[64:79], v[180:183], v[224:227], v[64:79]
	ds_read_b64_tr_b16 v[224:225], v153 offset:12288
	ds_read_b64_tr_b16 v[226:227], v153 offset:14336
	s_waitcnt lgkmcnt(15)
	v_mfma_f32_32x32x16_bf16 v[48:63], v[180:183], v[234:237], v[48:63]
	ds_read_b64_tr_b16 v[234:235], v153 offset:12800
	ds_read_b64_tr_b16 v[236:237], v153 offset:14848
	s_waitcnt lgkmcnt(15)
	v_mfma_f32_32x32x16_bf16 v[32:47], v[180:183], v[238:241], v[32:47]
	ds_read_b64_tr_b16 v[238:239], v153 offset:13312
	ds_read_b64_tr_b16 v[240:241], v153 offset:15360
	s_waitcnt lgkmcnt(15)
	v_mfma_f32_32x32x16_bf16 v[16:31], v[180:183], v[242:245], v[16:31]
	ds_read_b64_tr_b16 v[242:243], v153 offset:13824
	ds_read_b64_tr_b16 v[244:245], v153 offset:15872
	ds_read_b128 v[180:183], v152 offset:32
	s_waitcnt lgkmcnt(15)
	v_mfma_f32_32x32x16_bf16 v[64:79], v[184:187], v[208:211], v[64:79]
	ds_read_b128 v[208:211], v246
	s_waitcnt lgkmcnt(15)
	v_mfma_f32_32x32x16_bf16 v[48:63], v[184:187], v[212:215], v[48:63]
	ds_read_b128 v[212:215], v246 offset:8192
	s_waitcnt lgkmcnt(15)
	v_mfma_f32_32x32x16_bf16 v[32:47], v[184:187], v[216:219], v[32:47]
	ds_read_b128 v[216:219], v247
	s_waitcnt lgkmcnt(14)
	v_mfma_f32_32x32x16_bf16 v[16:31], v[184:187], v[220:223], v[16:31]
	ds_read_b128 v[220:223], v247 offset:8192
	ds_read_b128 v[184:187], v152 offset:64
	s_waitcnt lgkmcnt(12)
	v_mfma_f32_32x32x16_bf16 v[64:79], v[188:191], v[224:227], v[64:79]
	ds_read_b128 v[224:227], v248
	s_waitcnt lgkmcnt(11)
	v_mfma_f32_32x32x16_bf16 v[48:63], v[188:191], v[234:237], v[48:63]
	ds_read_b128 v[234:237], v248 offset:8192
	s_waitcnt lgkmcnt(10)
	v_mfma_f32_32x32x16_bf16 v[32:47], v[188:191], v[238:241], v[32:47]
	ds_read_b128 v[238:241], v249
	s_waitcnt lgkmcnt(9)
	v_mfma_f32_32x32x16_bf16 v[16:31], v[188:191], v[242:245], v[16:31]
	ds_read_b128 v[242:245], v249 offset:8192
	ds_read_b128 v[188:191], v152 offset:96
	s_branch .Lat_turn_end1

.Lat_wd1:
	s_and_b64 vcc, exec, s[2:3]
	s_cbranch_vccnz .Lat_next1
	s_add_i32 s6, s45, 2
	s_cmp_ge_u32 s6, s46
	s_cbranch_scc1 .Lat_next1
	s_and_b32 s7, s6, 3
	s_lshl_b32 s7, s7, 8
	v_add_u32_e32 v0, s7, v171
	ds_write_b32 v0, v172

.LBB0_1250:
	s_cmpk_lt_i32 s67, 0x1080
	s_mov_b32 s60, s78
	s_waitcnt vmcnt(0) lgkmcnt(0)
	s_barrier
	v_mbcnt_lo_u32_b32 v20, -1, 0
	v_mbcnt_hi_u32_b32 v20, -1, v20
	s_cbranch_scc0 .LBB0_1259
	s_cmp_gt_u32 s67, 63
	s_cbranch_scc1 .LBB0_1259
	s_mov_b32 s63, s67
	v_readlane_b32 s7, v250, 43
	v_readlane_b32 s20, v250, 46
	v_readlane_b32 s21, v250, 47
	v_readlane_b32 s36, v250, 48
	v_readlane_b32 s37, v250, 49
	s_lshr_b32 s28, s63, 4
	s_and_b32 s29, s63, 15
	s_mul_i32 s30, s28, 0x1080
	s_lshl_b32 s29, s29, 8
	s_mul_i32 s33, s63, 0x4200
	s_add_u32 s42, s74, s33
	s_addc_u32 s43, s75, 0
	s_add_u32 s42, s42, 0x500000
	s_addc_u32 s43, s43, 0
	s_lshl_b32 s33, s7, 3
	s_add_i32 s33, s33, 0x1c0
	v_mov_b32_e32 v54, s33
	global_load_dwordx2 v[18:19], v54, s[42:43]
	v_lshrrev_b32_e32 v55, 2, v20
	v_lshlrev_b32_e32 v56, 2, v55
	global_load_dword v57, v56, s[42:43] offset:448
	s_add_i32 s31, s30, 0x70
	s_lshl_b32 s31, s31, 12
	s_add_i32 s31, s31, s29
	v_and_b32_e32 v58, 3, v20
	v_lshlrev_b32_e32 v58, 6, v58
	v_lshl_add_u32 v59, v55, 12, v58
	v_add_u32_e32 v59, s31, v59
	global_load_dwordx4 v[2:5], v59, s[24:25]
	global_load_dwordx4 v[6:9], v59, s[24:25] offset:16
	global_load_dwordx4 v[10:13], v59, s[24:25] offset:32
	global_load_dwordx4 v[14:17], v59, s[24:25] offset:48
	s_lshl_b32 s34, s7, 13
	s_add_i32 s34, s34, s31
	v_add_u32_e32 v60, s34, v58
	v_add_u32_e32 v61, 0x1000, v60
	global_load_dwordx4 v[22:25], v60, s[20:21]
	global_load_dwordx4 v[26:29], v60, s[20:21] offset:16
	global_load_dwordx4 v[30:33], v60, s[20:21] offset:32
	global_load_dwordx4 v[34:37], v60, s[20:21] offset:48
	global_load_dwordx4 v[38:41], v61, s[20:21]
	global_load_dwordx4 v[42:45], v61, s[20:21] offset:16
	global_load_dwordx4 v[46:49], v61, s[20:21] offset:32
	global_load_dwordx4 v[50:53], v61, s[20:21] offset:48
	v_lshlrev_b32_e32 v62, 2, v20
	v_add_u32_e32 v62, s31, v62
	global_load_dword v64, v62, s[26:27]
	v_add_u32_e32 v62, 0x1000, v62
	global_load_dword v65, v62, s[26:27]
	v_add_u32_e32 v62, 0x1000, v62
	global_load_dword v66, v62, s[26:27]
	v_add_u32_e32 v62, 0x1000, v62
	global_load_dword v67, v62, s[26:27]
	v_add_u32_e32 v62, 0x1000, v62
	global_load_dword v68, v62, s[26:27]
	v_add_u32_e32 v62, 0x1000, v62
	global_load_dword v69, v62, s[26:27]
	v_add_u32_e32 v62, 0x1000, v62
	global_load_dword v70, v62, s[26:27]
	v_add_u32_e32 v62, 0x1000, v62
	global_load_dword v71, v62, s[26:27]
	v_add_u32_e32 v62, 0x1000, v62
	global_load_dword v72, v62, s[26:27]
	v_add_u32_e32 v62, 0x1000, v62
	global_load_dword v73, v62, s[26:27]
	v_add_u32_e32 v62, 0x1000, v62
	global_load_dword v74, v62, s[26:27]
	v_add_u32_e32 v62, 0x1000, v62
	global_load_dword v75, v62, s[26:27]
	v_add_u32_e32 v62, 0x1000, v62
	global_load_dword v76, v62, s[26:27]
	v_add_u32_e32 v62, 0x1000, v62
	global_load_dword v77, v62, s[26:27]
	v_add_u32_e32 v62, 0x1000, v62
	global_load_dword v78, v62, s[26:27]
	v_add_u32_e32 v62, 0x1000, v62
	global_load_dword v79, v62, s[26:27]
	s_mul_i32 s35, s7, 6
	s_add_i32 s35, s35, s30
	s_add_i32 s35, s35, 64
	s_lshl_b32 s35, s35, 12
	s_add_i32 s35, s35, s29
	v_lshlrev_b32_e32 v63, 2, v20
	v_add_u32_e32 v63, s35, v63
	v_mov_b32_e32 v80, 0
	global_store_dword v63, v80, s[36:37]
	v_add_u32_e32 v63, 0x1000, v63
	global_store_dword v63, v80, s[36:37]
	v_add_u32_e32 v63, 0x1000, v63
	global_store_dword v63, v80, s[36:37]
	v_add_u32_e32 v63, 0x1000, v63
	global_store_dword v63, v80, s[36:37]
	v_add_u32_e32 v63, 0x1000, v63
	global_store_dword v63, v80, s[36:37]
	v_add_u32_e32 v63, 0x1000, v63
	global_store_dword v63, v80, s[36:37]
	s_waitcnt vmcnt(0)
	v_mov_b32_e32 v81, 0
	v_mov_b32_e32 v82, 0
	v_lshlrev_b32_e32 v83, 16, v2
	v_and_b32_e32 v84, 0xffff0000, v2
	v_lshlrev_b32_e32 v85, 16, v22
	v_and_b32_e32 v86, 0xffff0000, v22
	v_fmac_f32_e32 v81, v83, v85
	v_fmac_f32_e32 v81, v84, v86
	v_lshlrev_b32_e32 v85, 16, v38
	v_and_b32_e32 v86, 0xffff0000, v38
	v_fmac_f32_e32 v82, v83, v85
	v_fmac_f32_e32 v82, v84, v86
	v_lshlrev_b32_e32 v83, 16, v3
	v_and_b32_e32 v84, 0xffff0000, v3
	v_lshlrev_b32_e32 v85, 16, v23
	v_and_b32_e32 v86, 0xffff0000, v23
	v_fmac_f32_e32 v81, v83, v85
	v_fmac_f32_e32 v81, v84, v86
	v_lshlrev_b32_e32 v85, 16, v39
	v_and_b32_e32 v86, 0xffff0000, v39
	v_fmac_f32_e32 v82, v83, v85
	v_fmac_f32_e32 v82, v84, v86
	v_lshlrev_b32_e32 v83, 16, v4
	v_and_b32_e32 v84, 0xffff0000, v4
	v_lshlrev_b32_e32 v85, 16, v24
	v_and_b32_e32 v86, 0xffff0000, v24
	v_fmac_f32_e32 v81, v83, v85
	v_fmac_f32_e32 v81, v84, v86
	v_lshlrev_b32_e32 v85, 16, v40
	v_and_b32_e32 v86, 0xffff0000, v40
	v_fmac_f32_e32 v82, v83, v85
	v_fmac_f32_e32 v82, v84, v86
	v_lshlrev_b32_e32 v83, 16, v5
	v_and_b32_e32 v84, 0xffff0000, v5
	v_lshlrev_b32_e32 v85, 16, v25
	v_and_b32_e32 v86, 0xffff0000, v25
	v_fmac_f32_e32 v81, v83, v85
	v_fmac_f32_e32 v81, v84, v86
	v_lshlrev_b32_e32 v85, 16, v41
	v_and_b32_e32 v86, 0xffff0000, v41
	v_fmac_f32_e32 v82, v83, v85
	v_fmac_f32_e32 v82, v84, v86
	v_lshlrev_b32_e32 v83, 16, v6
	v_and_b32_e32 v84, 0xffff0000, v6
	v_lshlrev_b32_e32 v85, 16, v26
	v_and_b32_e32 v86, 0xffff0000, v26
	v_fmac_f32_e32 v81, v83, v85
	v_fmac_f32_e32 v81, v84, v86
	v_lshlrev_b32_e32 v85, 16, v42
	v_and_b32_e32 v86, 0xffff0000, v42
	v_fmac_f32_e32 v82, v83, v85
	v_fmac_f32_e32 v82, v84, v86
	v_lshlrev_b32_e32 v83, 16, v7
	v_and_b32_e32 v84, 0xffff0000, v7
	v_lshlrev_b32_e32 v85, 16, v27
	v_and_b32_e32 v86, 0xffff0000, v27
	v_fmac_f32_e32 v81, v83, v85
	v_fmac_f32_e32 v81, v84, v86
	v_lshlrev_b32_e32 v85, 16, v43
	v_and_b32_e32 v86, 0xffff0000, v43
	v_fmac_f32_e32 v82, v83, v85
	v_fmac_f32_e32 v82, v84, v86
	v_lshlrev_b32_e32 v83, 16, v8
	v_and_b32_e32 v84, 0xffff0000, v8
	v_lshlrev_b32_e32 v85, 16, v28
	v_and_b32_e32 v86, 0xffff0000, v28
	v_fmac_f32_e32 v81, v83, v85
	v_fmac_f32_e32 v81, v84, v86
	v_lshlrev_b32_e32 v85, 16, v44
	v_and_b32_e32 v86, 0xffff0000, v44
	v_fmac_f32_e32 v82, v83, v85
	v_fmac_f32_e32 v82, v84, v86
	v_lshlrev_b32_e32 v83, 16, v9
	v_and_b32_e32 v84, 0xffff0000, v9
	v_lshlrev_b32_e32 v85, 16, v29
	v_and_b32_e32 v86, 0xffff0000, v29
	v_fmac_f32_e32 v81, v83, v85
	v_fmac_f32_e32 v81, v84, v86
	v_lshlrev_b32_e32 v85, 16, v45
	v_and_b32_e32 v86, 0xffff0000, v45
	v_fmac_f32_e32 v82, v83, v85
	v_fmac_f32_e32 v82, v84, v86
	v_lshlrev_b32_e32 v83, 16, v10
	v_and_b32_e32 v84, 0xffff0000, v10
	v_lshlrev_b32_e32 v85, 16, v30
	v_and_b32_e32 v86, 0xffff0000, v30
	v_fmac_f32_e32 v81, v83, v85
	v_fmac_f32_e32 v81, v84, v86
	v_lshlrev_b32_e32 v85, 16, v46
	v_and_b32_e32 v86, 0xffff0000, v46
	v_fmac_f32_e32 v82, v83, v85
	v_fmac_f32_e32 v82, v84, v86
	v_lshlrev_b32_e32 v83, 16, v11
	v_and_b32_e32 v84, 0xffff0000, v11
	v_lshlrev_b32_e32 v85, 16, v31
	v_and_b32_e32 v86, 0xffff0000, v31
	v_fmac_f32_e32 v81, v83, v85
	v_fmac_f32_e32 v81, v84, v86
	v_lshlrev_b32_e32 v85, 16, v47
	v_and_b32_e32 v86, 0xffff0000, v47
	v_fmac_f32_e32 v82, v83, v85
	v_fmac_f32_e32 v82, v84, v86
	v_lshlrev_b32_e32 v83, 16, v12
	v_and_b32_e32 v84, 0xffff0000, v12
	v_lshlrev_b32_e32 v85, 16, v32
	v_and_b32_e32 v86, 0xffff0000, v32
	v_fmac_f32_e32 v81, v83, v85
	v_fmac_f32_e32 v81, v84, v86
	v_lshlrev_b32_e32 v85, 16, v48
	v_and_b32_e32 v86, 0xffff0000, v48
	v_fmac_f32_e32 v82, v83, v85
	v_fmac_f32_e32 v82, v84, v86
	v_lshlrev_b32_e32 v83, 16, v13
	v_and_b32_e32 v84, 0xffff0000, v13
	v_lshlrev_b32_e32 v85, 16, v33
	v_and_b32_e32 v86, 0xffff0000, v33
	v_fmac_f32_e32 v81, v83, v85
	v_fmac_f32_e32 v81, v84, v86
	v_lshlrev_b32_e32 v85, 16, v49
	v_and_b32_e32 v86, 0xffff0000, v49
	v_fmac_f32_e32 v82, v83, v85
	v_fmac_f32_e32 v82, v84, v86
	v_lshlrev_b32_e32 v83, 16, v14
	v_and_b32_e32 v84, 0xffff0000, v14
	v_lshlrev_b32_e32 v85, 16, v34
	v_and_b32_e32 v86, 0xffff0000, v34
	v_fmac_f32_e32 v81, v83, v85
	v_fmac_f32_e32 v81, v84, v86
	v_lshlrev_b32_e32 v85, 16, v50
	v_and_b32_e32 v86, 0xffff0000, v50
	v_fmac_f32_e32 v82, v83, v85
	v_fmac_f32_e32 v82, v84, v86
	v_lshlrev_b32_e32 v83, 16, v15
	v_and_b32_e32 v84, 0xffff0000, v15
	v_lshlrev_b32_e32 v85, 16, v35
	v_and_b32_e32 v86, 0xffff0000, v35
	v_fmac_f32_e32 v81, v83, v85
	v_fmac_f32_e32 v81, v84, v86
	v_lshlrev_b32_e32 v85, 16, v51
	v_and_b32_e32 v86, 0xffff0000, v51
	v_fmac_f32_e32 v82, v83, v85
	v_fmac_f32_e32 v82, v84, v86
	v_lshlrev_b32_e32 v83, 16, v16
	v_and_b32_e32 v84, 0xffff0000, v16
	v_lshlrev_b32_e32 v85, 16, v36
	v_and_b32_e32 v86, 0xffff0000, v36
	v_fmac_f32_e32 v81, v83, v85
	v_fmac_f32_e32 v81, v84, v86
	v_lshlrev_b32_e32 v85, 16, v52
	v_and_b32_e32 v86, 0xffff0000, v52
	v_fmac_f32_e32 v82, v83, v85
	v_fmac_f32_e32 v82, v84, v86
	v_lshlrev_b32_e32 v83, 16, v17
	v_and_b32_e32 v84, 0xffff0000, v17
	v_lshlrev_b32_e32 v85, 16, v37
	v_and_b32_e32 v86, 0xffff0000, v37
	v_fmac_f32_e32 v81, v83, v85
	v_fmac_f32_e32 v81, v84, v86
	v_lshlrev_b32_e32 v85, 16, v53
	v_and_b32_e32 v86, 0xffff0000, v53
	v_fmac_f32_e32 v82, v83, v85
	v_fmac_f32_e32 v82, v84, v86
	s_nop 1
	v_add_f32_dpp v81, v81, v81 quad_perm:[1,0,3,2] row_mask:0xf bank_mask:0xf
	s_nop 1
	v_add_f32_dpp v81, v81, v81 quad_perm:[2,3,0,1] row_mask:0xf bank_mask:0xf
	s_nop 1
	v_add_f32_dpp v82, v82, v82 quad_perm:[1,0,3,2] row_mask:0xf bank_mask:0xf
	s_nop 1
	v_add_f32_dpp v82, v82, v82 quad_perm:[2,3,0,1] row_mask:0xf bank_mask:0xf
	s_mov_b32 s38, 0x3db504f3
	s_mov_b32 s40, 0x3fb8aa3b
	s_lshl_b32 s39, s7, 1
	v_mov_b32_e32 v99, 0xff800000
	v_sub_f32_e32 v87, v18, v57
	v_fma_f32 v81, v81, s38, v87
	v_cmp_ge_u32_e32 vcc, s39, v55
	s_nop 1
	v_cndmask_b32_e32 v81, v99, v81, vcc
	v_mov_b32_e32 v88, v81
	s_nop 1
	v_max_f32_dpp v88, v88, v88 row_ror:4 row_mask:0xf bank_mask:0xf
	s_nop 1
	v_max_f32_dpp v88, v88, v88 row_ror:8 row_mask:0xf bank_mask:0xf
	s_nop 1
	v_readlane_b32 s46, v88, 0
	v_readlane_b32 s47, v88, 16
	v_readlane_b32 s48, v88, 32
	v_readlane_b32 s49, v88, 48
	v_mov_b32_e32 v89, s46
	v_max_f32_e32 v89, s47, v89
	v_max_f32_e32 v89, s48, v89
	v_max_f32_e32 v89, s49, v89
	v_sub_f32_e32 v81, v81, v89
	v_mul_f32_e32 v81, s40, v81
	v_exp_f32_e32 v81, v81
	s_nop 0
	v_mov_b32_e32 v90, v81
	s_nop 1
	v_add_f32_dpp v90, v90, v90 row_ror:4 row_mask:0xf bank_mask:0xf
	s_nop 1
	v_add_f32_dpp v90, v90, v90 row_ror:8 row_mask:0xf bank_mask:0xf
	s_nop 1
	v_readlane_b32 s46, v90, 0
	v_readlane_b32 s47, v90, 16
	v_readlane_b32 s48, v90, 32
	v_readlane_b32 s49, v90, 48
	v_mov_b32_e32 v91, s46
	v_add_f32_e32 v91, s47, v91
	v_add_f32_e32 v91, s48, v91
	v_add_f32_e32 v91, s49, v91
	v_readlane_b32 s4, v81, 0
	v_readlane_b32 s5, v81, 4
	v_readlane_b32 s6, v81, 8
	v_readlane_b32 s7, v81, 12
	v_readlane_b32 s8, v81, 16
	v_readlane_b32 s9, v81, 20
	v_readlane_b32 s10, v81, 24
	v_readlane_b32 s11, v81, 28
	v_readlane_b32 s12, v81, 32
	v_readlane_b32 s13, v81, 36
	v_readlane_b32 s14, v81, 40
	v_readlane_b32 s15, v81, 44
	v_readlane_b32 s16, v81, 48
	v_readlane_b32 s17, v81, 52
	v_readlane_b32 s18, v81, 56
	v_readlane_b32 s19, v81, 60
	v_mov_b32_e32 v92, 0
	v_mov_b32_e32 v93, 0
	v_lshlrev_b32_e32 v94, 16, v64
	v_and_b32_e32 v95, 0xffff0000, v64
	v_fmac_f32_e32 v92, s4, v94
	v_fmac_f32_e32 v93, s4, v95
	v_lshlrev_b32_e32 v94, 16, v65
	v_and_b32_e32 v95, 0xffff0000, v65
	v_fmac_f32_e32 v92, s5, v94
	v_fmac_f32_e32 v93, s5, v95
	v_lshlrev_b32_e32 v94, 16, v66
	v_and_b32_e32 v95, 0xffff0000, v66
	v_fmac_f32_e32 v92, s6, v94
	v_fmac_f32_e32 v93, s6, v95
	v_lshlrev_b32_e32 v94, 16, v67
	v_and_b32_e32 v95, 0xffff0000, v67
	v_fmac_f32_e32 v92, s7, v94
	v_fmac_f32_e32 v93, s7, v95
	v_lshlrev_b32_e32 v94, 16, v68
	v_and_b32_e32 v95, 0xffff0000, v68
	v_fmac_f32_e32 v92, s8, v94
	v_fmac_f32_e32 v93, s8, v95
	v_lshlrev_b32_e32 v94, 16, v69
	v_and_b32_e32 v95, 0xffff0000, v69
	v_fmac_f32_e32 v92, s9, v94
	v_fmac_f32_e32 v93, s9, v95
	v_lshlrev_b32_e32 v94, 16, v70
	v_and_b32_e32 v95, 0xffff0000, v70
	v_fmac_f32_e32 v92, s10, v94
	v_fmac_f32_e32 v93, s10, v95
	v_lshlrev_b32_e32 v94, 16, v71
	v_and_b32_e32 v95, 0xffff0000, v71
	v_fmac_f32_e32 v92, s11, v94
	v_fmac_f32_e32 v93, s11, v95
	v_lshlrev_b32_e32 v94, 16, v72
	v_and_b32_e32 v95, 0xffff0000, v72
	v_fmac_f32_e32 v92, s12, v94
	v_fmac_f32_e32 v93, s12, v95
	v_lshlrev_b32_e32 v94, 16, v73
	v_and_b32_e32 v95, 0xffff0000, v73
	v_fmac_f32_e32 v92, s13, v94
	v_fmac_f32_e32 v93, s13, v95
	v_lshlrev_b32_e32 v94, 16, v74
	v_and_b32_e32 v95, 0xffff0000, v74
	v_fmac_f32_e32 v92, s14, v94
	v_fmac_f32_e32 v93, s14, v95
	v_lshlrev_b32_e32 v94, 16, v75
	v_and_b32_e32 v95, 0xffff0000, v75
	v_fmac_f32_e32 v92, s15, v94
	v_fmac_f32_e32 v93, s15, v95
	v_lshlrev_b32_e32 v94, 16, v76
	v_and_b32_e32 v95, 0xffff0000, v76
	v_fmac_f32_e32 v92, s16, v94
	v_fmac_f32_e32 v93, s16, v95
	v_lshlrev_b32_e32 v94, 16, v77
	v_and_b32_e32 v95, 0xffff0000, v77
	v_fmac_f32_e32 v92, s17, v94
	v_fmac_f32_e32 v93, s17, v95
	v_lshlrev_b32_e32 v94, 16, v78
	v_and_b32_e32 v95, 0xffff0000, v78
	v_fmac_f32_e32 v92, s18, v94
	v_fmac_f32_e32 v93, s18, v95
	v_lshlrev_b32_e32 v94, 16, v79
	v_and_b32_e32 v95, 0xffff0000, v79
	v_fmac_f32_e32 v92, s19, v94
	v_fmac_f32_e32 v93, s19, v95
	v_div_scale_f32 v96, s[46:47], v91, v91, 1.0
	v_rcp_f32_e32 v97, v96
	v_div_scale_f32 v98, vcc, 1.0, v91, 1.0
	v_fma_f32 v100, -v96, v97, 1.0
	v_fmac_f32_e32 v97, v100, v97
	v_mul_f32_e32 v100, v98, v97
	v_fma_f32 v101, -v96, v100, v98
	v_fmac_f32_e32 v100, v101, v97
	v_fma_f32 v96, -v96, v100, v98
	s_nop 1
	v_div_fmas_f32 v96, v96, v97, v100
	v_div_fixup_f32 v96, v96, v91, 1.0
	v_cmp_lt_f32_e32 vcc, 0, v91
	s_nop 1
	v_cndmask_b32_e32 v96, 0, v96, vcc
	v_mul_f32_e32 v92, v92, v96
	v_mul_f32_e32 v93, v93, v96
	v_cvt_pk_bf16_f32 v92, v92, v93
	v_lshlrev_b32_e32 v102, 2, v20
	v_add_u32_e32 v102, s34, v102
	global_store_dword v102, v92, s[36:37]
	v_sub_f32_e32 v87, v19, v57
	v_fma_f32 v82, v82, s38, v87
	s_add_i32 s39, s39, 1
	v_cmp_ge_u32_e32 vcc, s39, v55
	s_nop 1
	v_cndmask_b32_e32 v82, v99, v82, vcc
	v_mov_b32_e32 v88, v82
	s_nop 1
	v_max_f32_dpp v88, v88, v88 row_ror:4 row_mask:0xf bank_mask:0xf
	s_nop 1
	v_max_f32_dpp v88, v88, v88 row_ror:8 row_mask:0xf bank_mask:0xf
	s_nop 1
	v_readlane_b32 s46, v88, 0
	v_readlane_b32 s47, v88, 16
	v_readlane_b32 s48, v88, 32
	v_readlane_b32 s49, v88, 48
	v_mov_b32_e32 v89, s46
	v_max_f32_e32 v89, s47, v89
	v_max_f32_e32 v89, s48, v89
	v_max_f32_e32 v89, s49, v89
	v_sub_f32_e32 v82, v82, v89
	v_mul_f32_e32 v82, s40, v82
	v_exp_f32_e32 v82, v82
	s_nop 0
	v_mov_b32_e32 v90, v82
	s_nop 1
	v_add_f32_dpp v90, v90, v90 row_ror:4 row_mask:0xf bank_mask:0xf
	s_nop 1
	v_add_f32_dpp v90, v90, v90 row_ror:8 row_mask:0xf bank_mask:0xf
	s_nop 1
	v_readlane_b32 s46, v90, 0
	v_readlane_b32 s47, v90, 16
	v_readlane_b32 s48, v90, 32
	v_readlane_b32 s49, v90, 48
	v_mov_b32_e32 v91, s46
	v_add_f32_e32 v91, s47, v91
	v_add_f32_e32 v91, s48, v91
	v_add_f32_e32 v91, s49, v91
	v_readlane_b32 s4, v82, 0
	v_readlane_b32 s5, v82, 4
	v_readlane_b32 s6, v82, 8
	v_readlane_b32 s7, v82, 12
	v_readlane_b32 s8, v82, 16
	v_readlane_b32 s9, v82, 20
	v_readlane_b32 s10, v82, 24
	v_readlane_b32 s11, v82, 28
	v_readlane_b32 s12, v82, 32
	v_readlane_b32 s13, v82, 36
	v_readlane_b32 s14, v82, 40
	v_readlane_b32 s15, v82, 44
	v_readlane_b32 s16, v82, 48
	v_readlane_b32 s17, v82, 52
	v_readlane_b32 s18, v82, 56
	v_readlane_b32 s19, v82, 60
	v_mov_b32_e32 v92, 0
	v_mov_b32_e32 v93, 0
	v_lshlrev_b32_e32 v94, 16, v64
	v_and_b32_e32 v95, 0xffff0000, v64
	v_fmac_f32_e32 v92, s4, v94
	v_fmac_f32_e32 v93, s4, v95
	v_lshlrev_b32_e32 v94, 16, v65
	v_and_b32_e32 v95, 0xffff0000, v65
	v_fmac_f32_e32 v92, s5, v94
	v_fmac_f32_e32 v93, s5, v95
	v_lshlrev_b32_e32 v94, 16, v66
	v_and_b32_e32 v95, 0xffff0000, v66
	v_fmac_f32_e32 v92, s6, v94
	v_fmac_f32_e32 v93, s6, v95
	v_lshlrev_b32_e32 v94, 16, v67
	v_and_b32_e32 v95, 0xffff0000, v67
	v_fmac_f32_e32 v92, s7, v94
	v_fmac_f32_e32 v93, s7, v95
	v_lshlrev_b32_e32 v94, 16, v68
	v_and_b32_e32 v95, 0xffff0000, v68
	v_fmac_f32_e32 v92, s8, v94
	v_fmac_f32_e32 v93, s8, v95
	v_lshlrev_b32_e32 v94, 16, v69
	v_and_b32_e32 v95, 0xffff0000, v69
	v_fmac_f32_e32 v92, s9, v94
	v_fmac_f32_e32 v93, s9, v95
	v_lshlrev_b32_e32 v94, 16, v70
	v_and_b32_e32 v95, 0xffff0000, v70
	v_fmac_f32_e32 v92, s10, v94
	v_fmac_f32_e32 v93, s10, v95
	v_lshlrev_b32_e32 v94, 16, v71
	v_and_b32_e32 v95, 0xffff0000, v71
	v_fmac_f32_e32 v92, s11, v94
	v_fmac_f32_e32 v93, s11, v95
	v_lshlrev_b32_e32 v94, 16, v72
	v_and_b32_e32 v95, 0xffff0000, v72
	v_fmac_f32_e32 v92, s12, v94
	v_fmac_f32_e32 v93, s12, v95
	v_lshlrev_b32_e32 v94, 16, v73
	v_and_b32_e32 v95, 0xffff0000, v73
	v_fmac_f32_e32 v92, s13, v94
	v_fmac_f32_e32 v93, s13, v95
	v_lshlrev_b32_e32 v94, 16, v74
	v_and_b32_e32 v95, 0xffff0000, v74
	v_fmac_f32_e32 v92, s14, v94
	v_fmac_f32_e32 v93, s14, v95
	v_lshlrev_b32_e32 v94, 16, v75
	v_and_b32_e32 v95, 0xffff0000, v75
	v_fmac_f32_e32 v92, s15, v94
	v_fmac_f32_e32 v93, s15, v95
	v_lshlrev_b32_e32 v94, 16, v76
	v_and_b32_e32 v95, 0xffff0000, v76
	v_fmac_f32_e32 v92, s16, v94
	v_fmac_f32_e32 v93, s16, v95
	v_lshlrev_b32_e32 v94, 16, v77
	v_and_b32_e32 v95, 0xffff0000, v77
	v_fmac_f32_e32 v92, s17, v94
	v_fmac_f32_e32 v93, s17, v95
	v_lshlrev_b32_e32 v94, 16, v78
	v_and_b32_e32 v95, 0xffff0000, v78
	v_fmac_f32_e32 v92, s18, v94
	v_fmac_f32_e32 v93, s18, v95
	v_lshlrev_b32_e32 v94, 16, v79
	v_and_b32_e32 v95, 0xffff0000, v79
	v_fmac_f32_e32 v92, s19, v94
	v_fmac_f32_e32 v93, s19, v95
	v_div_scale_f32 v96, s[46:47], v91, v91, 1.0
	v_rcp_f32_e32 v97, v96
	v_div_scale_f32 v98, vcc, 1.0, v91, 1.0
	v_fma_f32 v100, -v96, v97, 1.0
	v_fmac_f32_e32 v97, v100, v97
	v_mul_f32_e32 v100, v98, v97
	v_fma_f32 v101, -v96, v100, v98
	v_fmac_f32_e32 v100, v101, v97
	v_fma_f32 v96, -v96, v100, v98
	s_nop 1
	v_div_fmas_f32 v96, v96, v97, v100
	v_div_fixup_f32 v96, v96, v91, 1.0
	v_cmp_lt_f32_e32 vcc, 0, v91
	s_nop 1
	v_cndmask_b32_e32 v96, 0, v96, vcc
	v_mul_f32_e32 v92, v92, v96
	v_mul_f32_e32 v93, v93, v96
	v_cvt_pk_bf16_f32 v92, v92, v93
	v_lshlrev_b32_e32 v102, 2, v20
	s_add_i32 s34, s34, 0x1000
	v_add_u32_e32 v102, s34, v102
	global_store_dword v102, v92, s[36:37]
	s_branch .LBB0_1259
